# baseline (speedup 1.0000x reference)
.LBB1_52:
	s_or_b64 exec, exec, s[8:9]
	v_lshlrev_b32_e32 v1, 1, v0
	s_movk_i32 s8, 0xc4
	v_cmp_gt_u32_e64 s[10:11], s8, v0
	v_mov_b32_e32 v53, 0
	v_lshlrev_b32_e32 v56, 2, v1
	v_mov_b32_e32 v55, 0
	s_waitcnt lgkmcnt(0)
	s_barrier
	s_and_saveexec_b64 s[8:9], s[10:11]
	ds_read_b32 v55, v56 offset:4160
	s_or_b64 exec, exec, s[8:9]
	v_or_b32_e32 v54, 1, v1
	s_movk_i32 s8, 0x187
	v_cmp_gt_u32_e64 s[8:9], s8, v54
	s_and_saveexec_b64 s[12:13], s[8:9]
	ds_read_b32 v53, v56 offset:4164
	s_or_b64 exec, exec, s[12:13]
	s_waitcnt lgkmcnt(0)
	v_add_u32_e32 v56, v53, v55
	v_mov_b32_e32 v60, v55
	v_mov_b32_e32 v61, v53
	v_lshlrev_b32_e32 v64, 8, v0
	s_and_saveexec_b64 s[12:13], s[10:11]
	global_atomic_add_x2 v[62:63], v64, v[60:61], s[16:17] sc0
	s_mov_b64 exec, s[12:13]
	v_mov_b32_e32 v57, 0
	v_cmp_ne_u32_e64 s[12:13], 0, v0
	v_mov_b32_e32 v58, 0
	ds_write_b32 v40, v56
	s_waitcnt lgkmcnt(0)
	s_barrier
	s_and_saveexec_b64 s[14:15], s[12:13]
	v_add_u32_e32 v58, -4, v40
	ds_read_b32 v58, v58
	s_or_b64 exec, exec, s[14:15]
	s_waitcnt lgkmcnt(0)
	s_barrier
	ds_read_b32 v59, v40
	v_cmp_lt_u32_e64 s[12:13], 1, v0
	s_waitcnt lgkmcnt(0)
	v_add_u32_e32 v58, v59, v58
	ds_write_b32 v40, v58
	s_waitcnt lgkmcnt(0)
	s_barrier
	s_and_saveexec_b64 s[14:15], s[12:13]
	v_add_u32_e32 v57, -8, v40
	ds_read_b32 v57, v57
	s_or_b64 exec, exec, s[14:15]
	s_waitcnt lgkmcnt(0)
	s_barrier
	ds_read_b32 v58, v40
	v_cmp_lt_u32_e64 s[12:13], 3, v0
	s_waitcnt lgkmcnt(0)
	v_add_u32_e32 v57, v58, v57
	ds_write_b32 v40, v57
	v_mov_b32_e32 v57, 0
	v_mov_b32_e32 v58, 0
	s_waitcnt lgkmcnt(0)
	s_barrier
	s_and_saveexec_b64 s[14:15], s[12:13]
	v_add_u32_e32 v58, -16, v40
	ds_read_b32 v58, v58
	s_or_b64 exec, exec, s[14:15]
	s_waitcnt lgkmcnt(0)
	s_barrier
	ds_read_b32 v59, v40
	v_cmp_lt_u32_e64 s[12:13], 7, v0
	s_waitcnt lgkmcnt(0)
	v_add_u32_e32 v58, v59, v58
	ds_write_b32 v40, v58
	s_waitcnt lgkmcnt(0)
	s_barrier
	s_and_saveexec_b64 s[14:15], s[12:13]
	v_subrev_u32_e32 v57, 32, v40
	ds_read_b32 v57, v57
	s_or_b64 exec, exec, s[14:15]
	s_waitcnt lgkmcnt(0)
	s_barrier
	ds_read_b32 v58, v40
	v_cmp_lt_u32_e64 s[12:13], 15, v0
	s_waitcnt lgkmcnt(0)
	v_add_u32_e32 v57, v58, v57
	ds_write_b32 v40, v57
	v_mov_b32_e32 v57, 0
	v_mov_b32_e32 v58, 0
	s_waitcnt lgkmcnt(0)
	s_barrier
	s_and_saveexec_b64 s[14:15], s[12:13]
	v_subrev_u32_e32 v58, 64, v40
	ds_read_b32 v58, v58
	s_or_b64 exec, exec, s[14:15]
	s_waitcnt lgkmcnt(0)
	s_barrier
	ds_read_b32 v59, v40
	v_cmp_lt_u32_e64 s[12:13], 31, v0
	s_waitcnt lgkmcnt(0)
	v_add_u32_e32 v58, v59, v58
	ds_write_b32 v40, v58
	s_waitcnt lgkmcnt(0)
	s_barrier
	s_and_saveexec_b64 s[14:15], s[12:13]
	v_add_u32_e32 v57, 0xffffff80, v40
	ds_read_b32 v57, v57
	s_or_b64 exec, exec, s[14:15]
	s_waitcnt lgkmcnt(0)
	s_barrier
	ds_read_b32 v58, v40
	v_cmp_lt_u32_e64 s[12:13], 63, v0
	s_waitcnt lgkmcnt(0)
	v_add_u32_e32 v57, v58, v57
	ds_write_b32 v40, v57
	v_mov_b32_e32 v57, 0
	v_mov_b32_e32 v58, 0
	s_waitcnt lgkmcnt(0)
	s_barrier
	s_and_saveexec_b64 s[14:15], s[12:13]
	v_add_u32_e32 v58, 0xffffff00, v40
	ds_read_b32 v58, v58
	s_or_b64 exec, exec, s[14:15]
	s_waitcnt lgkmcnt(0)
	s_barrier
	ds_read_b32 v59, v40
	s_movk_i32 s12, 0x7f
	v_cmp_lt_u32_e64 s[12:13], s12, v0
	s_waitcnt lgkmcnt(0)
	v_add_u32_e32 v58, v59, v58
	ds_write_b32 v40, v58
	s_waitcnt lgkmcnt(0)
	s_barrier
	s_and_saveexec_b64 s[14:15], s[12:13]
	v_add_u32_e32 v57, 0xfffffe00, v40
	ds_read_b32 v57, v57
	s_or_b64 exec, exec, s[14:15]
	s_waitcnt lgkmcnt(0)
	s_barrier
	ds_read_b32 v58, v40
	s_waitcnt lgkmcnt(0)
	v_add_u32_e32 v57, v58, v57
	ds_write_b32 v40, v57
	s_waitcnt lgkmcnt(0)
	s_barrier
	ds_read_b32 v57, v40
	v_add_u32_e32 v40, v40, v34
	s_waitcnt lgkmcnt(0)
	s_barrier
	v_sub_u32_e32 v56, v57, v56
	s_and_saveexec_b64 s[12:13], s[10:11]
	s_cbranch_execz .LBB1_80
	ds_write_b32 v40, v56 offset:1024
	v_add_u32_e32 v58, v56, v55
	s_and_saveexec_b64 s[14:15], s[8:9]
	ds_write_b32 v40, v58 offset:1028

.LBB1_87:
	v_lshlrev_b32_e32 v2, 2, v39
	v_mov_b32_e32 v3, 1
	ds_add_rtn_u32 v2, v2, v3 offset:4160
	v_lshlrev_b32_e32 v4, 17, v6
	s_mov_b32 s2, 0x1fe0000
	s_waitcnt vmcnt(1)
	v_and_or_b32 v4, v4, s2, v30
	s_waitcnt lgkmcnt(0)
	v_lshlrev_b32_e32 v5, 2, v2
	v_lshlrev_b32_e32 v2, 1, v2
	v_sub_u32_e32 v2, v5, v2
	ds_write_b32 v5, v4 offset:5728
	ds_write_b16 v2, v39 offset:22112
	v_lshlrev_b32_e32 v2, 2, v38
	ds_add_rtn_u32 v2, v2, v3 offset:4160
	v_lshlrev_b32_e32 v4, 17, v7
	v_and_or_b32 v4, v4, s2, v31
	s_waitcnt lgkmcnt(0)
	v_lshlrev_b32_e32 v5, 2, v2
	v_lshlrev_b32_e32 v2, 1, v2
	v_sub_u32_e32 v2, v5, v2
	ds_write_b32 v5, v4 offset:5728
	ds_write_b16 v2, v38 offset:22112
	v_lshlrev_b32_e32 v2, 2, v37
	ds_add_rtn_u32 v2, v2, v3 offset:4160
	v_lshlrev_b32_e32 v4, 17, v8
	v_and_or_b32 v4, v4, s2, v32
	s_waitcnt lgkmcnt(0)
	v_lshlrev_b32_e32 v5, 2, v2
	v_lshlrev_b32_e32 v2, 1, v2
	v_sub_u32_e32 v2, v5, v2
	ds_write_b32 v5, v4 offset:5728
	ds_write_b16 v2, v37 offset:22112
	v_lshlrev_b32_e32 v2, 2, v35
	ds_add_rtn_u32 v2, v2, v3 offset:4160
	v_lshlrev_b32_e32 v3, 17, v9
	v_and_or_b32 v3, v3, s2, v33
	s_waitcnt lgkmcnt(0)
	v_lshlrev_b32_e32 v4, 2, v2
	v_lshlrev_b32_e32 v2, 1, v2
	v_sub_u32_e32 v2, v4, v2
	ds_write_b32 v4, v3 offset:5728
	ds_write_b16 v2, v35 offset:22112
.LBB1_88:
	s_or_b64 exec, exec, s[0:1]
	s_add_u32 s0, s16, 0xc380
	s_addc_u32 s1, s17, 0
	v_add_u32_e32 v6, 0x1660, v34
	s_mov_b64 s[2:3], 0
	s_movk_i32 s10, 0x17ff
	v_mov_b32_e32 v7, 0
	s_movk_i32 s11, 0x6000
	s_movk_i32 s36, 0xc4
	v_cmp_gt_u32_e64 s[38:39], s36, v0
	s_movk_i32 s36, 0xc3
	v_cmp_gt_u32_e64 s[40:41], s36, v0
	v_lshlrev_b32_e32 v64, 3, v0
	s_waitcnt vmcnt(0)
	s_and_saveexec_b64 s[36:37], s[38:39]
	ds_write_b32 v64, v62 offset:2592
	s_and_b64 exec, exec, s[40:41]
	ds_write_b32 v64, v63 offset:2596
	s_mov_b64 exec, s[36:37]
	s_waitcnt lgkmcnt(0)
	s_barrier
	s_branch .LBB1_90

.LBB1_97:
	v_lshlrev_b32_e32 v36, 2, v52
	v_mov_b32_e32 v40, 1
	ds_add_rtn_u32 v36, v36, v40 offset:4160
	v_lshlrev_b32_e32 v10, 17, v10
	s_mov_b32 s0, 0x1fe0000
	s_waitcnt vmcnt(1)
	v_and_or_b32 v10, v10, s0, v14
	v_lshlrev_b32_e32 v11, 17, v11
	s_waitcnt lgkmcnt(0)
	v_lshlrev_b32_e32 v14, 2, v36
	ds_write_b32 v14, v10 offset:5728
	v_lshlrev_b32_e32 v10, 1, v36
	v_sub_u32_e32 v10, v14, v10
	ds_write_b16 v10, v52 offset:22112
	v_lshlrev_b32_e32 v10, 2, v51
	ds_add_rtn_u32 v10, v10, v40 offset:4160
	v_and_or_b32 v11, v11, s0, v15
	s_waitcnt lgkmcnt(0)
	v_lshlrev_b32_e32 v14, 2, v10
	v_lshlrev_b32_e32 v10, 1, v10
	v_sub_u32_e32 v10, v14, v10
	ds_write_b32 v14, v11 offset:5728
	ds_write_b16 v10, v51 offset:22112
	v_lshlrev_b32_e32 v10, 2, v50
	ds_add_rtn_u32 v10, v10, v40 offset:4160
	v_lshlrev_b32_e32 v11, 17, v12
	v_and_or_b32 v11, v11, s0, v16
	s_waitcnt lgkmcnt(0)
	v_lshlrev_b32_e32 v12, 2, v10
	v_lshlrev_b32_e32 v10, 1, v10
	v_sub_u32_e32 v10, v12, v10
	ds_write_b32 v12, v11 offset:5728
	ds_write_b16 v10, v50 offset:22112
	v_lshlrev_b32_e32 v10, 2, v49
	ds_add_rtn_u32 v10, v10, v40 offset:4160
	v_lshlrev_b32_e32 v11, 17, v13
	v_and_or_b32 v11, v11, s0, v17
	s_waitcnt lgkmcnt(0)
	v_lshlrev_b32_e32 v12, 2, v10
	v_lshlrev_b32_e32 v10, 1, v10
	v_sub_u32_e32 v10, v12, v10
	ds_write_b32 v12, v11 offset:5728
	ds_write_b16 v10, v49 offset:22112
	s_or_b64 exec, exec, s[8:9]
	s_and_saveexec_b64 s[0:1], s[2:3]
	s_cbranch_execz .LBB1_85
.LBB1_98:
	v_lshlrev_b32_e32 v10, 2, v48
	v_mov_b32_e32 v11, 1
	ds_add_rtn_u32 v10, v10, v11 offset:4160
	v_lshlrev_b32_e32 v2, 17, v2
	s_mov_b32 s2, 0x1fe0000
	s_waitcnt vmcnt(1)
	v_and_or_b32 v2, v2, s2, v22
	v_lshlrev_b32_e32 v3, 17, v3
	s_waitcnt lgkmcnt(0)
	v_lshlrev_b32_e32 v12, 2, v10
	ds_write_b32 v12, v2 offset:5728
	v_lshlrev_b32_e32 v2, 1, v10
	v_sub_u32_e32 v2, v12, v2
	ds_write_b16 v2, v48 offset:22112
	v_lshlrev_b32_e32 v2, 2, v47
	ds_add_rtn_u32 v2, v2, v11 offset:4160
	v_and_or_b32 v3, v3, s2, v23
	s_waitcnt lgkmcnt(0)
	v_lshlrev_b32_e32 v10, 2, v2
	v_lshlrev_b32_e32 v2, 1, v2
	v_sub_u32_e32 v2, v10, v2
	ds_write_b32 v10, v3 offset:5728
	ds_write_b16 v2, v47 offset:22112
	v_lshlrev_b32_e32 v2, 2, v46
	ds_add_rtn_u32 v2, v2, v11 offset:4160
	v_lshlrev_b32_e32 v3, 17, v4
	v_and_or_b32 v3, v3, s2, v24
	s_waitcnt lgkmcnt(0)
	v_lshlrev_b32_e32 v4, 2, v2
	v_lshlrev_b32_e32 v2, 1, v2
	v_sub_u32_e32 v2, v4, v2
	ds_write_b32 v4, v3 offset:5728
	ds_write_b16 v2, v46 offset:22112
	v_lshlrev_b32_e32 v2, 2, v45
	ds_add_rtn_u32 v2, v2, v11 offset:4160
	v_lshlrev_b32_e32 v3, 17, v5
	v_and_or_b32 v3, v3, s2, v25
	s_waitcnt lgkmcnt(0)
	v_lshlrev_b32_e32 v4, 2, v2
	v_lshlrev_b32_e32 v2, 1, v2
	v_sub_u32_e32 v2, v4, v2
	ds_write_b32 v4, v3 offset:5728
	ds_write_b16 v2, v45 offset:22112
	s_or_b64 exec, exec, s[0:1]
	s_and_saveexec_b64 s[0:1], s[4:5]
	s_cbranch_execz .LBB1_86
.LBB1_99:
	v_lshlrev_b32_e32 v2, 2, v44
	v_mov_b32_e32 v3, 1
	ds_add_rtn_u32 v2, v2, v3 offset:4160
	v_lshlrev_b32_e32 v4, 17, v18
	s_mov_b32 s2, 0x1fe0000
	s_waitcnt vmcnt(1)
	v_and_or_b32 v4, v4, s2, v26
	s_waitcnt lgkmcnt(0)
	v_lshlrev_b32_e32 v5, 2, v2
	v_lshlrev_b32_e32 v2, 1, v2
	v_sub_u32_e32 v2, v5, v2
	ds_write_b32 v5, v4 offset:5728
	ds_write_b16 v2, v44 offset:22112
	v_lshlrev_b32_e32 v2, 2, v43
	ds_add_rtn_u32 v2, v2, v3 offset:4160
	v_lshlrev_b32_e32 v4, 17, v19
	v_and_or_b32 v4, v4, s2, v27
	s_waitcnt lgkmcnt(0)
	v_lshlrev_b32_e32 v5, 2, v2
	v_lshlrev_b32_e32 v2, 1, v2
	v_sub_u32_e32 v2, v5, v2
	ds_write_b32 v5, v4 offset:5728
	ds_write_b16 v2, v43 offset:22112
	v_lshlrev_b32_e32 v2, 2, v42
	ds_add_rtn_u32 v2, v2, v3 offset:4160
	v_lshlrev_b32_e32 v4, 17, v20
	v_and_or_b32 v4, v4, s2, v28
	s_waitcnt lgkmcnt(0)
	v_lshlrev_b32_e32 v5, 2, v2
	v_lshlrev_b32_e32 v2, 1, v2
	v_sub_u32_e32 v2, v5, v2
	ds_write_b32 v5, v4 offset:5728
	ds_write_b16 v2, v42 offset:22112
	v_lshlrev_b32_e32 v2, 2, v41
	ds_add_rtn_u32 v2, v2, v3 offset:4160
	v_lshlrev_b32_e32 v3, 17, v21
	v_and_or_b32 v3, v3, s2, v29
	s_waitcnt lgkmcnt(0)
	v_lshlrev_b32_e32 v4, 2, v2
	v_lshlrev_b32_e32 v2, 1, v2
	v_sub_u32_e32 v2, v4, v2
	ds_write_b32 v4, v3 offset:5728
	ds_write_b16 v2, v41 offset:22112
	s_or_b64 exec, exec, s[0:1]
	s_and_saveexec_b64 s[0:1], s[6:7]
	s_cbranch_execnz .LBB1_87
	s_branch .LBB1_88
